# MFMA-shadow interleave: the filler's f32->e4m3 conversion moved into the QK block's MFMA gaps (in place), on top of v55
# baseline (speedup 1.0000x reference)
; DEV int ltid() { int t = threadIdx.x; asm volatile("" : "+v"(t)); return t; }
; DEV void fill_store(CParams& p, int wg, int slot, int bufsel) {
;   extern __shared__ __attribute__((aligned(16))) char shm[];
;   const unsigned* T = (const unsigned*)(shm + FILL_LDS_OFF + bufsel * FILL_TB); const int tid = ltid(), nl = tid >> 3, cc = tid & 7;
;   const FillDesc d = fill_decode(p, wg, slot);
;   u32x4 v; v.x = T[nl * 33 + 4 * cc]; v.y = T[nl * 33 + 4 * cc + 1]; v.z = T[nl * 33 + 4 * cc + 2]; v.w = T[nl * 33 + 4 * cc + 3];
;   *(u32x4*)(d.dst + (long)perm_row(d.perm, d.n0 + nl) * 2048 + d.kh + 16 * cc) = v;
; }
.LBB0_899:
	s_xor_b32 s56, s36, 1
	s_mul_i32 s56, s56, 0x2200
	v_add_u32_e32 v76, s56, v244
	ds_read2_b32 v[72:73], v76 offset1:1
	ds_read2_b32 v[74:75], v76 offset0:2 offset1:3
	s_add_i32 s57, s37, 66
	s_cmp_gt_u32 s57, 0x7f
	s_cbranch_scc1 .Lfst_a_d
	s_lshr_b32 s58, s57, 2
	s_lshl_b32 s58, s58, 23
	s_and_b32 s59, s57, 3
	s_lshl_b32 s59, s59, 9
	s_or_b32 s58, s58, s59
	s_add_u32 s60, s12, s58
	s_addc_u32 s61, s13, 0
	s_waitcnt lgkmcnt(0)
	global_store_dwordx4 v246, v[72:75], s[60:61]
	s_branch .Lfst_a_end

; DEV void fill_write(const f32x4 (&ld)[4], int bufsel) {
;   extern __shared__ __attribute__((aligned(16))) char shm[];
; DEV void partialSM(f32x16& p0, f32x16& p1, float& m_reg, float& mn, float& alpha) {
;   constexpr float C = SCALE * 1.4426950408889634f;
;   float pmax = p0[0];
; #pragma unroll
;   for (int r = 1; r < 16; ++r) pmax = fmaxf(pmax, p0[r]);
; #pragma unroll
;   for (int r = 0; r < 16; ++r) pmax = fmaxf(pmax, p1[r]);
;   { auto rr = __builtin_amdgcn_permlane32_swap(__float_as_uint(pmax), __float_as_uint(pmax), false, false);
;     pmax = fmaxf(__uint_as_float(rr[0]), __uint_as_float(rr[1])); }
;   if (__builtin_expect(__all(pmax - m_reg <= THR / SCALE), 1)) { mn = m_reg; alpha = 1.f; }
;   else { mn = fmaxf(m_reg, pmax); alpha = __builtin_amdgcn_exp2f((m_reg - mn) * C); m_reg = mn; }
;   const float mnC = -mn * C;
; #pragma unroll
;   for (int r = 0; r < 16; ++r) p0[r] = fmaf(p0[r], C, mnC);
; #pragma unroll
;   for (int r = 0; r < 16; ++r) p1[r] = fmaf(p1[r], C, mnC);
; #pragma unroll
;   for (int r = 0; r < 16; ++r) p0[r] = __builtin_amdgcn_exp2f(p0[r]);
; }
; DEV void finishSM(f32x16& p0, f32x16& p1, float alpha, float& l_reg, bf16x8& pa0, bf16x8& pa1, bf16x8& pa2, bf16x8& pa3) {
; #pragma unroll
;   for (int r = 0; r < 16; ++r) p1[r] = __builtin_amdgcn_exp2f(p1[r]);
;   float ps = 0;
; #pragma unroll
;   for (int r = 0; r < 16; ++r) ps += p0[r];
; #pragma unroll
;   for (int r = 0; r < 16; ++r) ps += p1[r];
;   { auto rr = __builtin_amdgcn_permlane32_swap(__float_as_uint(ps), __float_as_uint(ps), false, false);
;     ps = __uint_as_float(rr[0]) + __uint_as_float(rr[1]); }
;   l_reg = l_reg * alpha + ps;
;     ...
;   PK4(p0, 0, pa0); PK4(p0, 8, pa1); PK4(p1, 0, pa2); PK4(p1, 8, pa3);
;     ...
; }
; DEV void qkt(f32x16& p0, f32x16& p1, const char* Ks, const bf16x8* qr, int r32, int hi) {
;   p0 = f32x16{}; p1 = f32x16{};
;   __builtin_amdgcn_s_setprio(1);
; #pragma unroll
;   for (int d0 = 0; d0 < 12; ++d0) { const int cb = (d0 * 16 + hi * 8) * 2;
;     const bf16x8 b0 = *reinterpret_cast<const bf16x8*>(Ks + KSWZ2(r32, cb));
;     const bf16x8 b1 = *reinterpret_cast<const bf16x8*>(Ks + KSWZ2(32 + r32, cb));
;     p0 = __builtin_amdgcn_mfma_f32_32x32x16_bf16(b0, qr[d0], p0, 0, 0, 0);
;     p1 = __builtin_amdgcn_mfma_f32_32x32x16_bf16(b1, qr[d0], p1, 0, 0, 0); }
;   __builtin_amdgcn_s_setprio(0);
; }
.Lfst_a_end:
.LBB0_907:
	s_lshl_b32 s6, s36, 15
	s_add_i32 s6, s6, 0
	s_setprio 1
	v_add3_u32 v66, s6, v201, v200
	ds_read_b128 v[68:71], v66 offset:32768
	ds_read_b128 v[72:75], v66 offset:49152
	v_add3_u32 v66, s6, v202, v200
	ds_read_b128 v[224:227], v66 offset:32768
	ds_read_b128 v[228:231], v66 offset:49152
	v_add3_u32 v66, s6, v203, v200
	s_waitcnt lgkmcnt(0)
	v_mfma_f32_32x32x16_bf16 v[84:99], v[68:71], v[100:103], 0
	v_mfma_f32_32x32x16_bf16 v[68:83], v[72:75], v[100:103], 0
	v_mfma_f32_32x32x16_bf16 v[84:99], v[224:227], v[104:107], v[84:99]
	v_mfma_f32_32x32x16_bf16 v[68:83], v[228:231], v[104:107], v[68:83]
	ds_read_b128 v[224:227], v66 offset:32768
	ds_read_b128 v[228:231], v66 offset:49152
	v_add3_u32 v66, s6, v204, v200
	s_waitcnt lgkmcnt(1)
	v_mfma_f32_32x32x16_bf16 v[84:99], v[224:227], v[108:111], v[84:99]
	s_waitcnt lgkmcnt(0)
	v_mfma_f32_32x32x16_bf16 v[68:83], v[228:231], v[108:111], v[68:83]
	ds_read_b128 v[224:227], v66 offset:32768
	ds_read_b128 v[228:231], v66 offset:49152
	v_add3_u32 v66, s6, v205, v200
	s_waitcnt lgkmcnt(1)
	v_mfma_f32_32x32x16_bf16 v[84:99], v[224:227], v[112:115], v[84:99]
	s_waitcnt lgkmcnt(0)
	v_mfma_f32_32x32x16_bf16 v[68:83], v[228:231], v[112:115], v[68:83]
	ds_read_b128 v[224:227], v66 offset:32768
	ds_read_b128 v[228:231], v66 offset:49152
	v_add3_u32 v66, s6, v206, v200
	s_waitcnt lgkmcnt(1)
	v_mfma_f32_32x32x16_bf16 v[84:99], v[224:227], v[116:119], v[84:99]
	s_waitcnt lgkmcnt(0)
	v_mfma_f32_32x32x16_bf16 v[68:83], v[228:231], v[116:119], v[68:83]
	s_waitcnt vmcnt(5)
	v_mul_f32_e32 v253, 0x42800000, v168
	v_mul_f32_e32 v254, 0x42800000, v172
	v_cvt_pk_fp8_f32 v168, v253, v254
	ds_read_b128 v[224:227], v66 offset:32768
	ds_read_b128 v[228:231], v66 offset:49152
	v_add3_u32 v66, s6, v207, v200
	s_waitcnt lgkmcnt(1)
	v_mfma_f32_32x32x16_bf16 v[84:99], v[224:227], v[120:123], v[84:99]
	s_waitcnt lgkmcnt(0)
	v_mfma_f32_32x32x16_bf16 v[68:83], v[228:231], v[120:123], v[68:83]
	v_mul_f32_e32 v253, 0x42800000, v176
	v_mul_f32_e32 v254, 0x42800000, v180
	v_cvt_pk_fp8_f32 v168, v253, v254 op_sel:[0,0,1]
	ds_read_b128 v[224:227], v66 offset:32768
	ds_read_b128 v[228:231], v66 offset:49152
	v_add3_u32 v66, s6, v208, v200
	s_waitcnt lgkmcnt(1)
	v_mfma_f32_32x32x16_bf16 v[84:99], v[224:227], v[124:127], v[84:99]
	s_waitcnt lgkmcnt(0)
	v_mfma_f32_32x32x16_bf16 v[68:83], v[228:231], v[124:127], v[68:83]
	v_mul_f32_e32 v253, 0x42800000, v169
	v_mul_f32_e32 v254, 0x42800000, v173
	v_cvt_pk_fp8_f32 v169, v253, v254
	ds_read_b128 v[224:227], v66 offset:32768
	ds_read_b128 v[228:231], v66 offset:49152
	v_add3_u32 v66, s6, v209, v200
	s_waitcnt lgkmcnt(1)
	v_mfma_f32_32x32x16_bf16 v[84:99], v[224:227], v[128:131], v[84:99]
	s_waitcnt lgkmcnt(0)
	v_mfma_f32_32x32x16_bf16 v[68:83], v[228:231], v[128:131], v[68:83]
	v_mul_f32_e32 v253, 0x42800000, v177
	v_mul_f32_e32 v254, 0x42800000, v181
	v_cvt_pk_fp8_f32 v169, v253, v254 op_sel:[0,0,1]
	ds_read_b128 v[224:227], v66 offset:32768
	ds_read_b128 v[228:231], v66 offset:49152
	v_add3_u32 v66, s6, v211, v200
	s_waitcnt lgkmcnt(1)
	v_mfma_f32_32x32x16_bf16 v[84:99], v[224:227], v[132:135], v[84:99]
	s_waitcnt lgkmcnt(0)
	v_mfma_f32_32x32x16_bf16 v[68:83], v[228:231], v[132:135], v[68:83]
	v_mul_f32_e32 v253, 0x42800000, v170
	v_mul_f32_e32 v254, 0x42800000, v174
	v_cvt_pk_fp8_f32 v170, v253, v254
	ds_read_b128 v[224:227], v66 offset:32768
	ds_read_b128 v[228:231], v66 offset:49152
	v_add3_u32 v66, s6, v212, v200
	s_waitcnt lgkmcnt(1)
	v_mfma_f32_32x32x16_bf16 v[84:99], v[224:227], v[140:143], v[84:99]
	s_waitcnt lgkmcnt(0)
	v_mfma_f32_32x32x16_bf16 v[68:83], v[228:231], v[140:143], v[68:83]
	v_mul_f32_e32 v253, 0x42800000, v178
	v_mul_f32_e32 v254, 0x42800000, v182
	v_cvt_pk_fp8_f32 v170, v253, v254 op_sel:[0,0,1]
	ds_read_b128 v[224:227], v66 offset:32768
	ds_read_b128 v[228:231], v66 offset:49152
	v_add3_u32 v66, s6, v213, v200
	s_waitcnt lgkmcnt(1)
	v_mfma_f32_32x32x16_bf16 v[84:99], v[224:227], v[136:139], v[84:99]
	s_waitcnt lgkmcnt(0)
	v_mfma_f32_32x32x16_bf16 v[68:83], v[228:231], v[136:139], v[68:83]
	v_mul_f32_e32 v253, 0x42800000, v171
	v_mul_f32_e32 v254, 0x42800000, v175
	v_cvt_pk_fp8_f32 v171, v253, v254
	ds_read_b128 v[224:227], v66 offset:32768
	ds_read_b128 v[228:231], v66 offset:49152
	s_waitcnt lgkmcnt(1)
	v_mfma_f32_32x32x16_bf16 v[84:99], v[224:227], v[144:147], v[84:99]
	s_waitcnt lgkmcnt(0)
	v_mfma_f32_32x32x16_bf16 v[68:83], v[228:231], v[144:147], v[68:83]
	v_mul_f32_e32 v253, 0x42800000, v179
	v_mul_f32_e32 v254, 0x42800000, v183
	v_cvt_pk_fp8_f32 v171, v253, v254 op_sel:[0,0,1]
	s_setprio 0
	s_nop 8
	v_max_f32_e32 v66, v85, v85
	v_max_f32_e32 v219, v84, v84
	v_max_f32_e32 v66, v219, v66
	v_max3_f32 v66, v66, v86, v87
	v_max3_f32 v66, v66, v88, v89
	v_max3_f32 v66, v66, v90, v91
	v_max3_f32 v66, v66, v92, v93
	v_max3_f32 v66, v66, v94, v95
	v_max3_f32 v66, v66, v96, v97
	v_max3_f32 v66, v66, v98, v99
	v_max3_f32 v66, v66, v68, v69
	v_max3_f32 v66, v66, v70, v71
	v_max3_f32 v66, v66, v72, v73
	v_max3_f32 v66, v66, v74, v75
	v_max3_f32 v66, v66, v76, v77
	v_max3_f32 v66, v66, v78, v79
	v_max3_f32 v66, v66, v80, v81
	v_max3_f32 v66, v66, v82, v83
	v_mov_b32_e32 v219, v66
	s_nop 1
	v_permlane32_swap_b32_e32 v66, v219
	v_max_f32_e32 v219, v219, v219
	v_max_f32_e32 v66, v66, v66
	v_max_f32_e32 v66, v66, v219
	v_max_f32_e32 v220, v215, v215
	v_sub_f32_e32 v219, v66, v215
	v_max_f32_e32 v66, v220, v66
	v_sub_f32_e32 v220, v215, v66
	v_mul_f32_e32 v220, 0x3dd53b94, v220
	v_exp_f32_e32 v220, v220
	v_cmp_ge_f32_e32 vcc, s31, v219
	s_cmp_eq_u64 vcc, exec
	s_cselect_b64 s[6:7], -1, 0
	v_cndmask_b32_e64 v219, v220, 1.0, s[6:7]
	v_cmp_gt_f32_e32 vcc, 1.0, v219
	s_cbranch_vccz .LBB0_911
; DEV void partialSM(f32x16& p0, f32x16& p1, float& m_reg, float& mn, float& alpha) {
;     ...
;   else { mn = fmaxf(m_reg, pmax); alpha = __builtin_amdgcn_exp2f((m_reg - mn) * C); m_reg = mn; }
;   const float mnC = -mn * C;
; #pragma unroll
;   for (int r = 0; r < 16; ++r) p0[r] = fmaf(p0[r], C, mnC);
; #pragma unroll
;   for (int r = 0; r < 16; ++r) p1[r] = fmaf(p1[r], C, mnC);
; #pragma unroll
;   for (int r = 0; r < 16; ++r) p0[r] = __builtin_amdgcn_exp2f(p0[r]);
; }
; DEV void finishSM(f32x16& p0, f32x16& p1, float alpha, float& l_reg, bf16x8& pa0, bf16x8& pa1, bf16x8& pa2, bf16x8& pa3) {
; #pragma unroll
;   for (int r = 0; r < 16; ++r) p1[r] = __builtin_amdgcn_exp2f(p1[r]);
;   float ps = 0;
; #pragma unroll
;   for (int r = 0; r < 16; ++r) ps += p0[r];
; #pragma unroll
;   for (int r = 0; r < 16; ++r) ps += p1[r];
;   { auto rr = __builtin_amdgcn_permlane32_swap(__float_as_uint(ps), __float_as_uint(ps), false, false);
;     ps = __uint_as_float(rr[0]) + __uint_as_float(rr[1]); }
;   l_reg = l_reg * alpha + ps;
;     ...
;   PK4(p0, 0, pa0); PK4(p0, 8, pa1); PK4(p1, 0, pa2); PK4(p1, 8, pa3);
;     ...
; }
; template <int OFF> DEV s16x4 tr_read(int vb) { s16x4 r; asm volatile("ds_read_b64_tr_b16 %0, %1 offset:%2" : "=&v"(r) : "v"(vb), "i"(OFF) : "memory"); return r; }
; template <int D0> DEV void pv_read(VFrag& f, int vb) {
;   f.l0 = tr_read<v_rd_off(D0, 0, 0)>(vb); f.h0 = tr_read<v_rd_off(D0, 0, 1)>(vb); f.l1 = tr_read<v_rd_off(D0, 1, 0)>(vb); f.h1 = tr_read<v_rd_off(D0, 1, 1)>(vb);
;   f.l2 = tr_read<v_rd_off(D0, 2, 0)>(vb); f.h2 = tr_read<v_rd_off(D0, 2, 1)>(vb); f.l3 = tr_read<v_rd_off(D0, 3, 0)>(vb); f.h3 = tr_read<v_rd_off(D0, 3, 1)>(vb);
	s_and_saveexec_b64 s[24:25], s[4:5]
	ds_write_b32 v210, v219 offset:128
	s_or_b64 exec, exec, s[24:25]
	s_waitcnt lgkmcnt(0)
	v_add_u32_e32 v220, v185, v186
	ds_read_b128 v[224:227], v220 offset:224
	ds_read_b128 v[228:231], v220 offset:192
	ds_read_b128 v[232:235], v220 offset:160
	ds_read_b128 v[236:239], v220 offset:128
	s_waitcnt lgkmcnt(3)
	v_pk_mul_f32 v[62:63], v[62:63], v[224:225]
	s_waitcnt lgkmcnt(2)
	v_pk_mul_f32 v[58:59], v[58:59], v[228:229]
	s_waitcnt lgkmcnt(1)
	v_pk_mul_f32 v[54:55], v[54:55], v[232:233]
	v_pk_mul_f32 v[64:65], v[64:65], v[226:227]
	v_pk_mul_f32 v[60:61], v[60:61], v[230:231]
	v_pk_mul_f32 v[56:57], v[56:57], v[234:235]
	s_waitcnt lgkmcnt(0)
	v_pk_mul_f32 v[52:53], v[52:53], v[238:239]
	v_pk_mul_f32 v[50:51], v[50:51], v[236:237]
	v_pk_mul_f32 v[46:47], v[46:47], v[224:225]
	v_pk_mul_f32 v[42:43], v[42:43], v[228:229]
	v_pk_mul_f32 v[38:39], v[38:39], v[232:233]
	v_pk_mul_f32 v[48:49], v[48:49], v[226:227]
	v_pk_mul_f32 v[44:45], v[44:45], v[230:231]
	v_pk_mul_f32 v[40:41], v[40:41], v[234:235]
	v_pk_mul_f32 v[36:37], v[36:37], v[238:239]
	v_pk_mul_f32 v[34:35], v[34:35], v[236:237]
	v_pk_mul_f32 v[30:31], v[30:31], v[224:225]
	v_pk_mul_f32 v[26:27], v[26:27], v[228:229]
	v_pk_mul_f32 v[22:23], v[22:23], v[232:233]
	v_pk_mul_f32 v[32:33], v[32:33], v[226:227]
	v_pk_mul_f32 v[28:29], v[28:29], v[230:231]
	v_pk_mul_f32 v[24:25], v[24:25], v[234:235]
	v_pk_mul_f32 v[20:21], v[20:21], v[238:239]
	v_pk_mul_f32 v[18:19], v[18:19], v[236:237]
	v_pk_mul_f32 v[14:15], v[14:15], v[224:225]
	v_pk_mul_f32 v[10:11], v[10:11], v[228:229]
	v_pk_mul_f32 v[6:7], v[6:7], v[232:233]
	v_pk_mul_f32 v[16:17], v[16:17], v[226:227]
	v_pk_mul_f32 v[12:13], v[12:13], v[230:231]
	v_pk_mul_f32 v[8:9], v[8:9], v[234:235]
	v_pk_mul_f32 v[4:5], v[4:5], v[238:239]
	v_pk_mul_f32 v[2:3], v[2:3], v[236:237]
.LBB0_911:
	v_cndmask_b32_e64 v215, v66, v215, s[6:7]
	v_mul_f32_e32 v66, 0xbdd53b94, v215
	v_fmamk_f32 v84, v84, 0x3dd53b94, v66
	v_fmamk_f32 v85, v85, 0x3dd53b94, v66
	v_fmamk_f32 v86, v86, 0x3dd53b94, v66
	v_fmamk_f32 v87, v87, 0x3dd53b94, v66
	v_fmamk_f32 v88, v88, 0x3dd53b94, v66
	v_fmamk_f32 v89, v89, 0x3dd53b94, v66
	v_fmamk_f32 v90, v90, 0x3dd53b94, v66
	v_fmamk_f32 v91, v91, 0x3dd53b94, v66
	v_fmamk_f32 v92, v92, 0x3dd53b94, v66
	v_fmamk_f32 v93, v93, 0x3dd53b94, v66
	v_fmamk_f32 v94, v94, 0x3dd53b94, v66
	v_fmamk_f32 v95, v95, 0x3dd53b94, v66
	v_fmamk_f32 v96, v96, 0x3dd53b94, v66
	v_fmamk_f32 v97, v97, 0x3dd53b94, v66
	v_fmamk_f32 v98, v98, 0x3dd53b94, v66
	v_fmamk_f32 v99, v99, 0x3dd53b94, v66
	v_fmamk_f32 v68, v68, 0x3dd53b94, v66
	v_fmamk_f32 v69, v69, 0x3dd53b94, v66
	v_fmamk_f32 v70, v70, 0x3dd53b94, v66
	v_fmamk_f32 v71, v71, 0x3dd53b94, v66
	v_fmamk_f32 v72, v72, 0x3dd53b94, v66
	v_fmamk_f32 v73, v73, 0x3dd53b94, v66
	v_fmamk_f32 v74, v74, 0x3dd53b94, v66
	v_fmamk_f32 v75, v75, 0x3dd53b94, v66
	v_fmamk_f32 v76, v76, 0x3dd53b94, v66
	v_fmamk_f32 v77, v77, 0x3dd53b94, v66
	v_fmamk_f32 v78, v78, 0x3dd53b94, v66
	v_fmamk_f32 v79, v79, 0x3dd53b94, v66
	v_fmamk_f32 v80, v80, 0x3dd53b94, v66
	v_fmamk_f32 v81, v81, 0x3dd53b94, v66
	v_fmamk_f32 v82, v82, 0x3dd53b94, v66
	v_fmac_f32_e32 v66, 0x3dd53b94, v83
	v_exp_f32_e32 v83, v84
	v_exp_f32_e32 v84, v85
	v_exp_f32_e32 v85, v86
	v_exp_f32_e32 v86, v87
	v_exp_f32_e32 v87, v88
	v_exp_f32_e32 v88, v89
	v_exp_f32_e32 v89, v90
	v_exp_f32_e32 v90, v91
	v_exp_f32_e32 v91, v92
	v_exp_f32_e32 v92, v93
	v_exp_f32_e32 v93, v94
	v_exp_f32_e32 v94, v95
	v_exp_f32_e32 v95, v96
	v_exp_f32_e32 v96, v97
	v_exp_f32_e32 v97, v98
	v_exp_f32_e32 v98, v99
	v_exp_f32_e32 v99, v68
	v_add_f32_e32 v68, 0, v83
	v_add_f32_e32 v68, v84, v68
	v_add_f32_e32 v68, v85, v68
	v_add_f32_e32 v68, v86, v68
	v_add_f32_e32 v68, v87, v68
	v_add_f32_e32 v68, v88, v68
	v_add_f32_e32 v68, v89, v68
	v_add_f32_e32 v68, v90, v68
	v_add_f32_e32 v68, v91, v68
	v_add_f32_e32 v68, v92, v68
	v_add_f32_e32 v68, v93, v68
	v_add_f32_e32 v68, v94, v68
	v_add_f32_e32 v68, v95, v68
	v_exp_f32_e32 v220, v69
	v_add_f32_e32 v68, v96, v68
	v_exp_f32_e32 v221, v70
	v_add_f32_e32 v68, v97, v68
	v_exp_f32_e32 v222, v71
	v_add_f32_e32 v68, v98, v68
	v_exp_f32_e32 v224, v72
	v_add_f32_e32 v68, v99, v68
	v_exp_f32_e32 v225, v73
	v_add_f32_e32 v68, v220, v68
	v_exp_f32_e32 v226, v74
	v_add_f32_e32 v68, v221, v68
	v_exp_f32_e32 v227, v75
	v_add_f32_e32 v68, v222, v68
	v_exp_f32_e32 v228, v76
	v_add_f32_e32 v68, v224, v68
	v_exp_f32_e32 v229, v77
	v_add_f32_e32 v68, v225, v68
	v_exp_f32_e32 v230, v78
	v_add_f32_e32 v68, v226, v68
	v_exp_f32_e32 v231, v79
	v_add_f32_e32 v68, v227, v68
	v_exp_f32_e32 v232, v80
	v_add_f32_e32 v68, v228, v68
	v_exp_f32_e32 v233, v81
	v_add_f32_e32 v68, v229, v68
	v_exp_f32_e32 v234, v82
	v_add_f32_e32 v68, v230, v68
	v_exp_f32_e32 v66, v66
	v_add_f32_e32 v68, v231, v68
	v_add_f32_e32 v68, v232, v68
	v_add_f32_e32 v68, v233, v68
	v_add_f32_e32 v68, v234, v68
	v_add_f32_e32 v68, v66, v68
	v_mov_b32_e32 v69, v68
	s_nop 1
	v_permlane32_swap_b32_e32 v68, v69
	v_cvt_pk_bf16_f32 v70, v83, v84
	v_cvt_pk_bf16_f32 v71, v85, v86
	v_cvt_pk_bf16_f32 v72, v87, v88
	v_cvt_pk_bf16_f32 v73, v89, v90
	v_cvt_pk_bf16_f32 v74, v91, v92
	v_cvt_pk_bf16_f32 v75, v93, v94
	v_cvt_pk_bf16_f32 v76, v95, v96
	v_cvt_pk_bf16_f32 v77, v97, v98
	v_cvt_pk_bf16_f32 v78, v99, v220
	v_cvt_pk_bf16_f32 v79, v221, v222
	v_cvt_pk_bf16_f32 v80, v224, v225
	v_cvt_pk_bf16_f32 v81, v226, v227
	v_cvt_pk_bf16_f32 v82, v228, v229
	v_cvt_pk_bf16_f32 v83, v230, v231
	v_cvt_pk_bf16_f32 v84, v232, v233
	v_cvt_pk_bf16_f32 v85, v234, v66
	v_permlane32_swap_b32_e32 v70, v72
	v_permlane32_swap_b32_e32 v71, v73
	v_permlane32_swap_b32_e32 v74, v76
	v_permlane32_swap_b32_e32 v75, v77
	v_permlane32_swap_b32_e32 v78, v80
	v_permlane32_swap_b32_e32 v79, v81
	v_permlane32_swap_b32_e32 v82, v84
	v_permlane32_swap_b32_e32 v83, v85
	v_lshl_add_u32 v66, s36, 14, v214
	ds_read_b64_tr_b16 v[86:87], v66 offset:0
	ds_read_b64_tr_b16 v[88:89], v66 offset:0x800
	ds_read_b64_tr_b16 v[90:91], v66 offset:0x1000
	ds_read_b64_tr_b16 v[92:93], v66 offset:0x1800
	ds_read_b64_tr_b16 v[94:95], v66 offset:0x2000
	ds_read_b64_tr_b16 v[96:97], v66 offset:0x2800
	ds_read_b64_tr_b16 v[224:225], v66 offset:0x3000
	ds_read_b64_tr_b16 v[226:227], v66 offset:0x3800
	ds_read_b64_tr_b16 v[228:229], v66 offset:0x200
	ds_read_b64_tr_b16 v[230:231], v66 offset:0xa00
	ds_read_b64_tr_b16 v[232:233], v66 offset:0x1200
	ds_read_b64_tr_b16 v[234:235], v66 offset:0x1a00
	ds_read_b64_tr_b16 v[236:237], v66 offset:0x2200
	ds_read_b64_tr_b16 v[238:239], v66 offset:0x2a00
	ds_read_b64_tr_b16 v[240:241], v66 offset:0x3200
	ds_read_b64_tr_b16 v[242:243], v66 offset:0x3a00
	s_waitcnt lgkmcnt(8)
; DEV int ltid() { int t = threadIdx.x; asm volatile("" : "+v"(t)); return t; }
; DEV unsigned cvt_pk4_fp8(f32x4 v) { unsigned r = 0; r = __builtin_amdgcn_cvt_pk_fp8_f32(v[0], v[1], r, false); r = __builtin_amdgcn_cvt_pk_fp8_f32(v[2], v[3], r, true); return r; }
; #define SBAR() __builtin_amdgcn_sched_barrier(0)
; #define PV_WAIT(n) do { asm volatile("s_waitcnt lgkmcnt(" #n ")" ::: "memory"); SBAR(); } while (0)
; DEV void fill_write(const f32x4 (&ld)[4], int bufsel) {
;   extern __shared__ __attribute__((aligned(16))) char shm[];
;   unsigned* T = (unsigned*)(shm + FILL_LDS_OFF + bufsel * FILL_TB); const int tid = ltid(), tx = tid & 15, ty = tid >> 4;
;   constexpr float WS = (float)(1 << FP8_WSCALE_LOG2_);
; #pragma unroll
;   for (int j = 0; j < 4; ++j) T[(4 * tx + j) * 33 + ty] = cvt_pk4_fp8((f32x4){ld[0][j] * WS, ld[1][j] * WS, ld[2][j] * WS, ld[3][j] * WS});
; }
; DEV void pv_mma(f32x16& od, const VFrag& f, bf16x8 pa0, bf16x8 pa1, bf16x8 pa2, bf16x8 pa3) {
;     ...
;   __builtin_amdgcn_s_setprio(1);
;   od = __builtin_amdgcn_mfma_f32_32x32x16_bf16(pa0, PK(f.l0, f.h0), od, 0, 0, 0);
;   od = __builtin_amdgcn_mfma_f32_32x32x16_bf16(pa1, PK(f.l1, f.h1), od, 0, 0, 0);
;   od = __builtin_amdgcn_mfma_f32_32x32x16_bf16(pa2, PK(f.l2, f.h2), od, 0, 0, 0);
;   od = __builtin_amdgcn_mfma_f32_32x32x16_bf16(pa3, PK(f.l3, f.h3), od, 0, 0, 0);
;   __builtin_amdgcn_s_setprio(0);
;     ...
; }
; DEV void pv_d0(f32x16* o, int vb, bf16x8 pa0, bf16x8 pa1, bf16x8 pa2, bf16x8 pa3) {
;   VFrag fa, fb;
;   pv_read<0>(fa, vb);
;   pv_read<1>(fb, vb); PV_WAIT(8); pv_mma(o[0], fa, pa0, pa1, pa2, pa3); SBAR();
;   pv_read<2>(fa, vb); PV_WAIT(8); pv_mma(o[1], fb, pa0, pa1, pa2, pa3); SBAR();
;   pv_read<3>(fb, vb); PV_WAIT(8); pv_mma(o[2], fa, pa0, pa1, pa2, pa3); SBAR();
;   PV_WAIT(0); pv_mma(o[3], fb, pa0, pa1, pa2, pa3);
; }
	s_setprio 1
	v_mfma_f32_32x32x16_bf16 v[50:65], v[70:73], v[86:89], v[50:65]
	v_mfma_f32_32x32x16_bf16 v[50:65], v[74:77], v[90:93], v[50:65]
	v_mfma_f32_32x32x16_bf16 v[50:65], v[78:81], v[94:97], v[50:65]
	v_mfma_f32_32x32x16_bf16 v[50:65], v[82:85], v[224:227], v[50:65]
	s_setprio 0
	ds_read_b64_tr_b16 v[86:87], v66 offset:0x400
	ds_read_b64_tr_b16 v[88:89], v66 offset:0xc00
	ds_read_b64_tr_b16 v[90:91], v66 offset:0x1400
	ds_read_b64_tr_b16 v[92:93], v66 offset:0x1c00
	ds_read_b64_tr_b16 v[94:95], v66 offset:0x2400
	ds_read_b64_tr_b16 v[96:97], v66 offset:0x2c00
	ds_read_b64_tr_b16 v[224:225], v66 offset:0x3400
	ds_read_b64_tr_b16 v[226:227], v66 offset:0x3c00
	s_waitcnt lgkmcnt(8)
	s_setprio 1
	v_mfma_f32_32x32x16_bf16 v[34:49], v[70:73], v[228:231], v[34:49]
	v_mfma_f32_32x32x16_bf16 v[34:49], v[74:77], v[232:235], v[34:49]
	v_mfma_f32_32x32x16_bf16 v[34:49], v[78:81], v[236:239], v[34:49]
	v_mfma_f32_32x32x16_bf16 v[34:49], v[82:85], v[240:243], v[34:49]
	s_setprio 0
	ds_read_b64_tr_b16 v[228:229], v66 offset:0x600
	ds_read_b64_tr_b16 v[230:231], v66 offset:0xe00
	ds_read_b64_tr_b16 v[232:233], v66 offset:0x1600
	ds_read_b64_tr_b16 v[234:235], v66 offset:0x1e00
	ds_read_b64_tr_b16 v[236:237], v66 offset:0x2600
	ds_read_b64_tr_b16 v[238:239], v66 offset:0x2e00
	ds_read_b64_tr_b16 v[240:241], v66 offset:0x3600
	ds_read_b64_tr_b16 v[242:243], v66 offset:0x3e00
	s_waitcnt lgkmcnt(8)
	s_setprio 1
	v_mfma_f32_32x32x16_bf16 v[18:33], v[70:73], v[86:89], v[18:33]
	v_mfma_f32_32x32x16_bf16 v[18:33], v[74:77], v[90:93], v[18:33]
	v_mfma_f32_32x32x16_bf16 v[18:33], v[78:81], v[94:97], v[18:33]
	v_mfma_f32_32x32x16_bf16 v[18:33], v[82:85], v[224:227], v[18:33]
	s_setprio 0
	s_waitcnt lgkmcnt(0)
	s_setprio 1
	v_mfma_f32_32x32x16_bf16 v[2:17], v[70:73], v[228:231], v[2:17]
	v_mfma_f32_32x32x16_bf16 v[2:17], v[74:77], v[232:235], v[2:17]
	v_mfma_f32_32x32x16_bf16 v[2:17], v[78:81], v[236:239], v[2:17]
	v_mfma_f32_32x32x16_bf16 v[2:17], v[82:85], v[240:243], v[2:17]
	s_setprio 0
	s_cmp_gt_u32 s37, 62
	s_cbranch_scc1 .LBB0_919
	s_mul_i32 s56, s36, 0x2200
	s_cmp_eq_u32 s34, 60
	v_add_u32_e32 v66, s56, v245
	ds_write2_b32 v66, v168, v169 offset1:33
	ds_write2_b32 v66, v170, v171 offset0:66 offset1:99
	s_cbranch_scc1 .LBB0_919
	s_cmp_lg_u32 s37, 60
	s_cbranch_scc1 .Lfld_a
	s_mov_b64 s[62:63], s[20:21]
	v_mov_b32_e32 v248, v252
	v_add_u32_e32 v249, 0x2000, v252
	v_add_u32_e32 v250, 0x4000, v252
	v_add_u32_e32 v251, 0x6000, v252

; DEV void fill_write(const f32x4 (&ld)[4], int bufsel) {
;   extern __shared__ __attribute__((aligned(16))) char shm[];
; DEV void partialSM(f32x16& p0, f32x16& p1, float& m_reg, float& mn, float& alpha) {
;   constexpr float C = SCALE * 1.4426950408889634f;
;   float pmax = p0[0];
; #pragma unroll
;   for (int r = 1; r < 16; ++r) pmax = fmaxf(pmax, p0[r]);
; #pragma unroll
;   for (int r = 0; r < 16; ++r) pmax = fmaxf(pmax, p1[r]);
;   { auto rr = __builtin_amdgcn_permlane32_swap(__float_as_uint(pmax), __float_as_uint(pmax), false, false);
;     pmax = fmaxf(__uint_as_float(rr[0]), __uint_as_float(rr[1])); }
;   if (__builtin_expect(__all(pmax - m_reg <= THR / SCALE), 1)) { mn = m_reg; alpha = 1.f; }
;   else { mn = fmaxf(m_reg, pmax); alpha = __builtin_amdgcn_exp2f((m_reg - mn) * C); m_reg = mn; }
;   const float mnC = -mn * C;
; #pragma unroll
;   for (int r = 0; r < 16; ++r) p0[r] = fmaf(p0[r], C, mnC);
; #pragma unroll
;   for (int r = 0; r < 16; ++r) p1[r] = fmaf(p1[r], C, mnC);
; #pragma unroll
;   for (int r = 0; r < 16; ++r) p0[r] = __builtin_amdgcn_exp2f(p0[r]);
; }
; DEV void finishSM(f32x16& p0, f32x16& p1, float alpha, float& l_reg, bf16x8& pa0, bf16x8& pa1, bf16x8& pa2, bf16x8& pa3) {
; #pragma unroll
;   for (int r = 0; r < 16; ++r) p1[r] = __builtin_amdgcn_exp2f(p1[r]);
;   float ps = 0;
; #pragma unroll
;   for (int r = 0; r < 16; ++r) ps += p0[r];
; #pragma unroll
;   for (int r = 0; r < 16; ++r) ps += p1[r];
;   { auto rr = __builtin_amdgcn_permlane32_swap(__float_as_uint(ps), __float_as_uint(ps), false, false);
;     ps = __uint_as_float(rr[0]) + __uint_as_float(rr[1]); }
;   l_reg = l_reg * alpha + ps;
;     ...
;   PK4(p0, 0, pa0); PK4(p0, 8, pa1); PK4(p1, 0, pa2); PK4(p1, 8, pa3);
;     ...
; }
; DEV void qkt(f32x16& p0, f32x16& p1, const char* Ks, const bf16x8* qr, int r32, int hi) {
;   p0 = f32x16{}; p1 = f32x16{};
;   __builtin_amdgcn_s_setprio(1);
; #pragma unroll
;   for (int d0 = 0; d0 < 12; ++d0) { const int cb = (d0 * 16 + hi * 8) * 2;
;     const bf16x8 b0 = *reinterpret_cast<const bf16x8*>(Ks + KSWZ2(r32, cb));
;     const bf16x8 b1 = *reinterpret_cast<const bf16x8*>(Ks + KSWZ2(32 + r32, cb));
;     p0 = __builtin_amdgcn_mfma_f32_32x32x16_bf16(b0, qr[d0], p0, 0, 0, 0);
;     p1 = __builtin_amdgcn_mfma_f32_32x32x16_bf16(b1, qr[d0], p1, 0, 0, 0); }
;   __builtin_amdgcn_s_setprio(0);
; }
.LBB0_1106:
	s_xor_b32 s56, s37, 1
	s_mul_i32 s56, s56, 0x2200
	v_add_u32_e32 v76, s56, v244
	ds_read2_b32 v[72:73], v76 offset1:1
	ds_read2_b32 v[74:75], v76 offset0:2 offset1:3
	s_add_i32 s57, s38, 129
	s_sub_u32 s57, s57, 0x80
	s_lshr_b32 s58, s57, 1
	s_lshl_b32 s58, s58, 22
	s_and_b32 s59, s57, 1
	s_lshl_b32 s59, s59, 10
	s_or_b32 s58, s58, s59
	s_add_u32 s60, s14, s58
	s_addc_u32 s61, s15, 0
	s_waitcnt lgkmcnt(0)
	global_store_dwordx4 v247, v[72:75], s[60:61]
.LBB0_1114:
	s_lshl_b32 s6, s37, 15
	s_add_i32 s6, s6, 0
	s_setprio 1
	v_add3_u32 v66, s6, v201, v200
	ds_read_b128 v[68:71], v66 offset:32768
	ds_read_b128 v[72:75], v66 offset:49152
	v_add3_u32 v66, s6, v202, v200
	ds_read_b128 v[224:227], v66 offset:32768
	ds_read_b128 v[228:231], v66 offset:49152
	v_add3_u32 v66, s6, v203, v200
	s_waitcnt lgkmcnt(0)
	v_mfma_f32_32x32x16_bf16 v[84:99], v[68:71], v[100:103], 0
	v_mfma_f32_32x32x16_bf16 v[68:83], v[72:75], v[100:103], 0
	v_mfma_f32_32x32x16_bf16 v[84:99], v[224:227], v[104:107], v[84:99]
	v_mfma_f32_32x32x16_bf16 v[68:83], v[228:231], v[104:107], v[68:83]
	ds_read_b128 v[224:227], v66 offset:32768
	ds_read_b128 v[228:231], v66 offset:49152
	v_add3_u32 v66, s6, v204, v200
	s_waitcnt lgkmcnt(1)
	v_mfma_f32_32x32x16_bf16 v[84:99], v[224:227], v[108:111], v[84:99]
	s_waitcnt lgkmcnt(0)
	v_mfma_f32_32x32x16_bf16 v[68:83], v[228:231], v[108:111], v[68:83]
	ds_read_b128 v[224:227], v66 offset:32768
	ds_read_b128 v[228:231], v66 offset:49152
	v_add3_u32 v66, s6, v205, v200
	s_waitcnt lgkmcnt(1)
	v_mfma_f32_32x32x16_bf16 v[84:99], v[224:227], v[112:115], v[84:99]
	s_waitcnt lgkmcnt(0)
	v_mfma_f32_32x32x16_bf16 v[68:83], v[228:231], v[112:115], v[68:83]
	ds_read_b128 v[224:227], v66 offset:32768
	ds_read_b128 v[228:231], v66 offset:49152
	v_add3_u32 v66, s6, v206, v200
	s_waitcnt lgkmcnt(1)
	v_mfma_f32_32x32x16_bf16 v[84:99], v[224:227], v[116:119], v[84:99]
	s_waitcnt lgkmcnt(0)
	v_mfma_f32_32x32x16_bf16 v[68:83], v[228:231], v[116:119], v[68:83]
	s_waitcnt vmcnt(5)
	v_mul_f32_e32 v253, 0x42800000, v168
	v_mul_f32_e32 v254, 0x42800000, v172
	v_cvt_pk_fp8_f32 v168, v253, v254
	ds_read_b128 v[224:227], v66 offset:32768
	ds_read_b128 v[228:231], v66 offset:49152
	v_add3_u32 v66, s6, v207, v200
	s_waitcnt lgkmcnt(1)
	v_mfma_f32_32x32x16_bf16 v[84:99], v[224:227], v[120:123], v[84:99]
	s_waitcnt lgkmcnt(0)
	v_mfma_f32_32x32x16_bf16 v[68:83], v[228:231], v[120:123], v[68:83]
	v_mul_f32_e32 v253, 0x42800000, v176
	v_mul_f32_e32 v254, 0x42800000, v180
	v_cvt_pk_fp8_f32 v168, v253, v254 op_sel:[0,0,1]
	ds_read_b128 v[224:227], v66 offset:32768
	ds_read_b128 v[228:231], v66 offset:49152
	v_add3_u32 v66, s6, v208, v200
	s_waitcnt lgkmcnt(1)
	v_mfma_f32_32x32x16_bf16 v[84:99], v[224:227], v[124:127], v[84:99]
	s_waitcnt lgkmcnt(0)
	v_mfma_f32_32x32x16_bf16 v[68:83], v[228:231], v[124:127], v[68:83]
	v_mul_f32_e32 v253, 0x42800000, v169
	v_mul_f32_e32 v254, 0x42800000, v173
	v_cvt_pk_fp8_f32 v169, v253, v254
	ds_read_b128 v[224:227], v66 offset:32768
	ds_read_b128 v[228:231], v66 offset:49152
	v_add3_u32 v66, s6, v209, v200
	s_waitcnt lgkmcnt(1)
	v_mfma_f32_32x32x16_bf16 v[84:99], v[224:227], v[128:131], v[84:99]
	s_waitcnt lgkmcnt(0)
	v_mfma_f32_32x32x16_bf16 v[68:83], v[228:231], v[128:131], v[68:83]
	v_mul_f32_e32 v253, 0x42800000, v177
	v_mul_f32_e32 v254, 0x42800000, v181
	v_cvt_pk_fp8_f32 v169, v253, v254 op_sel:[0,0,1]
	ds_read_b128 v[224:227], v66 offset:32768
	ds_read_b128 v[228:231], v66 offset:49152
	v_add3_u32 v66, s6, v211, v200
	s_waitcnt lgkmcnt(1)
	v_mfma_f32_32x32x16_bf16 v[84:99], v[224:227], v[132:135], v[84:99]
	s_waitcnt lgkmcnt(0)
	v_mfma_f32_32x32x16_bf16 v[68:83], v[228:231], v[132:135], v[68:83]
	v_mul_f32_e32 v253, 0x42800000, v170
	v_mul_f32_e32 v254, 0x42800000, v174
	v_cvt_pk_fp8_f32 v170, v253, v254
	ds_read_b128 v[224:227], v66 offset:32768
	ds_read_b128 v[228:231], v66 offset:49152
	v_add3_u32 v66, s6, v212, v200
	s_waitcnt lgkmcnt(1)
	v_mfma_f32_32x32x16_bf16 v[84:99], v[224:227], v[140:143], v[84:99]
	s_waitcnt lgkmcnt(0)
	v_mfma_f32_32x32x16_bf16 v[68:83], v[228:231], v[140:143], v[68:83]
	v_mul_f32_e32 v253, 0x42800000, v178
	v_mul_f32_e32 v254, 0x42800000, v182
	v_cvt_pk_fp8_f32 v170, v253, v254 op_sel:[0,0,1]
	ds_read_b128 v[224:227], v66 offset:32768
	ds_read_b128 v[228:231], v66 offset:49152
	v_add3_u32 v66, s6, v213, v200
	s_waitcnt lgkmcnt(1)
	v_mfma_f32_32x32x16_bf16 v[84:99], v[224:227], v[136:139], v[84:99]
	s_waitcnt lgkmcnt(0)
	v_mfma_f32_32x32x16_bf16 v[68:83], v[228:231], v[136:139], v[68:83]
	v_mul_f32_e32 v253, 0x42800000, v171
	v_mul_f32_e32 v254, 0x42800000, v175
	v_cvt_pk_fp8_f32 v171, v253, v254
	ds_read_b128 v[224:227], v66 offset:32768
	ds_read_b128 v[228:231], v66 offset:49152
	s_waitcnt lgkmcnt(1)
	v_mfma_f32_32x32x16_bf16 v[84:99], v[224:227], v[144:147], v[84:99]
	s_waitcnt lgkmcnt(0)
	v_mfma_f32_32x32x16_bf16 v[68:83], v[228:231], v[144:147], v[68:83]
	v_mul_f32_e32 v253, 0x42800000, v179
	v_mul_f32_e32 v254, 0x42800000, v183
	v_cvt_pk_fp8_f32 v171, v253, v254 op_sel:[0,0,1]
	s_setprio 0
	s_nop 8
	v_max_f32_e32 v66, v85, v85
	v_max_f32_e32 v219, v84, v84
	v_max_f32_e32 v66, v219, v66
	v_max3_f32 v66, v66, v86, v87
	v_max3_f32 v66, v66, v88, v89
	v_max3_f32 v66, v66, v90, v91
	v_max3_f32 v66, v66, v92, v93
	v_max3_f32 v66, v66, v94, v95
	v_max3_f32 v66, v66, v96, v97
	v_max3_f32 v66, v66, v98, v99
	v_max3_f32 v66, v66, v68, v69
	v_max3_f32 v66, v66, v70, v71
	v_max3_f32 v66, v66, v72, v73
	v_max3_f32 v66, v66, v74, v75
	v_max3_f32 v66, v66, v76, v77
	v_max3_f32 v66, v66, v78, v79
	v_max3_f32 v66, v66, v80, v81
	v_max3_f32 v66, v66, v82, v83
	v_mov_b32_e32 v219, v66
	s_nop 1
	v_permlane32_swap_b32_e32 v66, v219
	v_max_f32_e32 v219, v219, v219
	v_max_f32_e32 v66, v66, v66
	v_max_f32_e32 v66, v66, v219
	v_max_f32_e32 v220, v215, v215
	v_sub_f32_e32 v219, v66, v215
	v_max_f32_e32 v66, v220, v66
	v_sub_f32_e32 v220, v215, v66
	v_mul_f32_e32 v220, 0x3dd53b94, v220
	v_exp_f32_e32 v220, v220
	v_cmp_ge_f32_e32 vcc, s34, v219
	s_cmp_eq_u64 vcc, exec
	s_cselect_b64 s[6:7], -1, 0
	v_cndmask_b32_e64 v219, v220, 1.0, s[6:7]
	v_cmp_gt_f32_e32 vcc, 1.0, v219
	s_cbranch_vccz .LBB0_1118
; DEV void partialSM(f32x16& p0, f32x16& p1, float& m_reg, float& mn, float& alpha) {
;     ...
;   else { mn = fmaxf(m_reg, pmax); alpha = __builtin_amdgcn_exp2f((m_reg - mn) * C); m_reg = mn; }
;   const float mnC = -mn * C;
; #pragma unroll
;   for (int r = 0; r < 16; ++r) p0[r] = fmaf(p0[r], C, mnC);
; #pragma unroll
;   for (int r = 0; r < 16; ++r) p1[r] = fmaf(p1[r], C, mnC);
; #pragma unroll
;   for (int r = 0; r < 16; ++r) p0[r] = __builtin_amdgcn_exp2f(p0[r]);
; }
; DEV void finishSM(f32x16& p0, f32x16& p1, float alpha, float& l_reg, bf16x8& pa0, bf16x8& pa1, bf16x8& pa2, bf16x8& pa3) {
; #pragma unroll
;   for (int r = 0; r < 16; ++r) p1[r] = __builtin_amdgcn_exp2f(p1[r]);
;   float ps = 0;
; #pragma unroll
;   for (int r = 0; r < 16; ++r) ps += p0[r];
; #pragma unroll
;   for (int r = 0; r < 16; ++r) ps += p1[r];
;   { auto rr = __builtin_amdgcn_permlane32_swap(__float_as_uint(ps), __float_as_uint(ps), false, false);
;     ps = __uint_as_float(rr[0]) + __uint_as_float(rr[1]); }
;   l_reg = l_reg * alpha + ps;
;     ...
;   PK4(p0, 0, pa0); PK4(p0, 8, pa1); PK4(p1, 0, pa2); PK4(p1, 8, pa3);
;     ...
; }
; template <int OFF> DEV s16x4 tr_read(int vb) { s16x4 r; asm volatile("ds_read_b64_tr_b16 %0, %1 offset:%2" : "=&v"(r) : "v"(vb), "i"(OFF) : "memory"); return r; }
; template <int D0> DEV void pv_read(VFrag& f, int vb) {
;   f.l0 = tr_read<v_rd_off(D0, 0, 0)>(vb); f.h0 = tr_read<v_rd_off(D0, 0, 1)>(vb); f.l1 = tr_read<v_rd_off(D0, 1, 0)>(vb); f.h1 = tr_read<v_rd_off(D0, 1, 1)>(vb);
;   f.l2 = tr_read<v_rd_off(D0, 2, 0)>(vb); f.h2 = tr_read<v_rd_off(D0, 2, 1)>(vb); f.l3 = tr_read<v_rd_off(D0, 3, 0)>(vb); f.h3 = tr_read<v_rd_off(D0, 3, 1)>(vb);
	s_and_saveexec_b64 s[26:27], s[4:5]
	ds_write_b32 v210, v219 offset:128
	s_or_b64 exec, exec, s[26:27]
	s_waitcnt lgkmcnt(0)
	v_add_u32_e32 v220, v185, v186
	ds_read_b128 v[224:227], v220 offset:224
	ds_read_b128 v[228:231], v220 offset:192
	ds_read_b128 v[232:235], v220 offset:160
	ds_read_b128 v[236:239], v220 offset:128
	s_waitcnt lgkmcnt(3)
	v_pk_mul_f32 v[62:63], v[62:63], v[224:225]
	s_waitcnt lgkmcnt(2)
	v_pk_mul_f32 v[58:59], v[58:59], v[228:229]
	s_waitcnt lgkmcnt(1)
	v_pk_mul_f32 v[54:55], v[54:55], v[232:233]
	v_pk_mul_f32 v[64:65], v[64:65], v[226:227]
	v_pk_mul_f32 v[60:61], v[60:61], v[230:231]
	v_pk_mul_f32 v[56:57], v[56:57], v[234:235]
	s_waitcnt lgkmcnt(0)
	v_pk_mul_f32 v[52:53], v[52:53], v[238:239]
	v_pk_mul_f32 v[50:51], v[50:51], v[236:237]
	v_pk_mul_f32 v[46:47], v[46:47], v[224:225]
	v_pk_mul_f32 v[42:43], v[42:43], v[228:229]
	v_pk_mul_f32 v[38:39], v[38:39], v[232:233]
	v_pk_mul_f32 v[48:49], v[48:49], v[226:227]
	v_pk_mul_f32 v[44:45], v[44:45], v[230:231]
	v_pk_mul_f32 v[40:41], v[40:41], v[234:235]
	v_pk_mul_f32 v[36:37], v[36:37], v[238:239]
	v_pk_mul_f32 v[34:35], v[34:35], v[236:237]
	v_pk_mul_f32 v[30:31], v[30:31], v[224:225]
	v_pk_mul_f32 v[26:27], v[26:27], v[228:229]
	v_pk_mul_f32 v[22:23], v[22:23], v[232:233]
	v_pk_mul_f32 v[32:33], v[32:33], v[226:227]
	v_pk_mul_f32 v[28:29], v[28:29], v[230:231]
	v_pk_mul_f32 v[24:25], v[24:25], v[234:235]
	v_pk_mul_f32 v[20:21], v[20:21], v[238:239]
	v_pk_mul_f32 v[18:19], v[18:19], v[236:237]
	v_pk_mul_f32 v[14:15], v[14:15], v[224:225]
	v_pk_mul_f32 v[10:11], v[10:11], v[228:229]
	v_pk_mul_f32 v[6:7], v[6:7], v[232:233]
	v_pk_mul_f32 v[16:17], v[16:17], v[226:227]
	v_pk_mul_f32 v[12:13], v[12:13], v[230:231]
	v_pk_mul_f32 v[8:9], v[8:9], v[234:235]
	v_pk_mul_f32 v[4:5], v[4:5], v[238:239]
	v_pk_mul_f32 v[2:3], v[2:3], v[236:237]
.LBB0_1118:
	v_cndmask_b32_e64 v215, v66, v215, s[6:7]
	v_mul_f32_e32 v66, 0xbdd53b94, v215
	v_fmamk_f32 v84, v84, 0x3dd53b94, v66
	v_fmamk_f32 v85, v85, 0x3dd53b94, v66
	v_fmamk_f32 v86, v86, 0x3dd53b94, v66
	v_fmamk_f32 v87, v87, 0x3dd53b94, v66
	v_fmamk_f32 v88, v88, 0x3dd53b94, v66
	v_fmamk_f32 v89, v89, 0x3dd53b94, v66
	v_fmamk_f32 v90, v90, 0x3dd53b94, v66
	v_fmamk_f32 v91, v91, 0x3dd53b94, v66
	v_fmamk_f32 v92, v92, 0x3dd53b94, v66
	v_fmamk_f32 v93, v93, 0x3dd53b94, v66
	v_fmamk_f32 v94, v94, 0x3dd53b94, v66
	v_fmamk_f32 v95, v95, 0x3dd53b94, v66
	v_fmamk_f32 v96, v96, 0x3dd53b94, v66
	v_fmamk_f32 v97, v97, 0x3dd53b94, v66
	v_fmamk_f32 v98, v98, 0x3dd53b94, v66
	v_fmamk_f32 v99, v99, 0x3dd53b94, v66
	v_fmamk_f32 v68, v68, 0x3dd53b94, v66
	v_fmamk_f32 v69, v69, 0x3dd53b94, v66
	v_fmamk_f32 v70, v70, 0x3dd53b94, v66
	v_fmamk_f32 v71, v71, 0x3dd53b94, v66
	v_fmamk_f32 v72, v72, 0x3dd53b94, v66
	v_fmamk_f32 v73, v73, 0x3dd53b94, v66
	v_fmamk_f32 v74, v74, 0x3dd53b94, v66
	v_fmamk_f32 v75, v75, 0x3dd53b94, v66
	v_fmamk_f32 v76, v76, 0x3dd53b94, v66
	v_fmamk_f32 v77, v77, 0x3dd53b94, v66
	v_fmamk_f32 v78, v78, 0x3dd53b94, v66
	v_fmamk_f32 v79, v79, 0x3dd53b94, v66
	v_fmamk_f32 v80, v80, 0x3dd53b94, v66
	v_fmamk_f32 v81, v81, 0x3dd53b94, v66
	v_fmamk_f32 v82, v82, 0x3dd53b94, v66
	v_fmac_f32_e32 v66, 0x3dd53b94, v83
	v_exp_f32_e32 v83, v84
	v_exp_f32_e32 v84, v85
	v_exp_f32_e32 v85, v86
	v_exp_f32_e32 v86, v87
	v_exp_f32_e32 v87, v88
	v_exp_f32_e32 v88, v89
	v_exp_f32_e32 v89, v90
	v_exp_f32_e32 v90, v91
	v_exp_f32_e32 v91, v92
	v_exp_f32_e32 v92, v93
	v_exp_f32_e32 v93, v94
	v_exp_f32_e32 v94, v95
	v_exp_f32_e32 v95, v96
	v_exp_f32_e32 v96, v97
	v_exp_f32_e32 v97, v98
	v_exp_f32_e32 v98, v99
	v_exp_f32_e32 v99, v68
	v_add_f32_e32 v68, 0, v83
	v_add_f32_e32 v68, v84, v68
	v_add_f32_e32 v68, v85, v68
	v_add_f32_e32 v68, v86, v68
	v_add_f32_e32 v68, v87, v68
	v_add_f32_e32 v68, v88, v68
	v_add_f32_e32 v68, v89, v68
	v_add_f32_e32 v68, v90, v68
	v_add_f32_e32 v68, v91, v68
	v_add_f32_e32 v68, v92, v68
	v_add_f32_e32 v68, v93, v68
	v_add_f32_e32 v68, v94, v68
	v_add_f32_e32 v68, v95, v68
	v_exp_f32_e32 v220, v69
	v_add_f32_e32 v68, v96, v68
	v_exp_f32_e32 v221, v70
	v_add_f32_e32 v68, v97, v68
	v_exp_f32_e32 v222, v71
	v_add_f32_e32 v68, v98, v68
	v_exp_f32_e32 v224, v72
	v_add_f32_e32 v68, v99, v68
	v_exp_f32_e32 v225, v73
	v_add_f32_e32 v68, v220, v68
	v_exp_f32_e32 v226, v74
	v_add_f32_e32 v68, v221, v68
	v_exp_f32_e32 v227, v75
	v_add_f32_e32 v68, v222, v68
	v_exp_f32_e32 v228, v76
	v_add_f32_e32 v68, v224, v68
	v_exp_f32_e32 v229, v77
	v_add_f32_e32 v68, v225, v68
	v_exp_f32_e32 v230, v78
	v_add_f32_e32 v68, v226, v68
	v_exp_f32_e32 v231, v79
	v_add_f32_e32 v68, v227, v68
	v_exp_f32_e32 v232, v80
	v_add_f32_e32 v68, v228, v68
	v_exp_f32_e32 v233, v81
	v_add_f32_e32 v68, v229, v68
	v_exp_f32_e32 v234, v82
	v_add_f32_e32 v68, v230, v68
	v_exp_f32_e32 v66, v66
	v_add_f32_e32 v68, v231, v68
	v_add_f32_e32 v68, v232, v68
	v_add_f32_e32 v68, v233, v68
	v_add_f32_e32 v68, v234, v68
	v_add_f32_e32 v68, v66, v68
	v_mov_b32_e32 v69, v68
	s_nop 1
	v_permlane32_swap_b32_e32 v68, v69
	v_cvt_pk_bf16_f32 v70, v83, v84
	v_cvt_pk_bf16_f32 v71, v85, v86
	v_cvt_pk_bf16_f32 v72, v87, v88
	v_cvt_pk_bf16_f32 v73, v89, v90
	v_cvt_pk_bf16_f32 v74, v91, v92
	v_cvt_pk_bf16_f32 v75, v93, v94
	v_cvt_pk_bf16_f32 v76, v95, v96
	v_cvt_pk_bf16_f32 v77, v97, v98
	v_cvt_pk_bf16_f32 v78, v99, v220
	v_cvt_pk_bf16_f32 v79, v221, v222
	v_cvt_pk_bf16_f32 v80, v224, v225
	v_cvt_pk_bf16_f32 v81, v226, v227
	v_cvt_pk_bf16_f32 v82, v228, v229
	v_cvt_pk_bf16_f32 v83, v230, v231
	v_cvt_pk_bf16_f32 v84, v232, v233
	v_cvt_pk_bf16_f32 v85, v234, v66
	v_permlane32_swap_b32_e32 v70, v72
	v_permlane32_swap_b32_e32 v71, v73
	v_permlane32_swap_b32_e32 v74, v76
	v_permlane32_swap_b32_e32 v75, v77
	v_permlane32_swap_b32_e32 v78, v80
	v_permlane32_swap_b32_e32 v79, v81
	v_permlane32_swap_b32_e32 v82, v84
	v_permlane32_swap_b32_e32 v83, v85
	v_lshl_add_u32 v66, s37, 14, v214
	ds_read_b64_tr_b16 v[86:87], v66 offset:0
	ds_read_b64_tr_b16 v[88:89], v66 offset:0x800
	ds_read_b64_tr_b16 v[90:91], v66 offset:0x1000
	ds_read_b64_tr_b16 v[92:93], v66 offset:0x1800
	ds_read_b64_tr_b16 v[94:95], v66 offset:0x2000
	ds_read_b64_tr_b16 v[96:97], v66 offset:0x2800
	ds_read_b64_tr_b16 v[224:225], v66 offset:0x3000
	ds_read_b64_tr_b16 v[226:227], v66 offset:0x3800
	ds_read_b64_tr_b16 v[228:229], v66 offset:0x200
	ds_read_b64_tr_b16 v[230:231], v66 offset:0xa00
	ds_read_b64_tr_b16 v[232:233], v66 offset:0x1200
	ds_read_b64_tr_b16 v[234:235], v66 offset:0x1a00
	ds_read_b64_tr_b16 v[236:237], v66 offset:0x2200
	ds_read_b64_tr_b16 v[238:239], v66 offset:0x2a00
	ds_read_b64_tr_b16 v[240:241], v66 offset:0x3200
	ds_read_b64_tr_b16 v[242:243], v66 offset:0x3a00
	s_waitcnt lgkmcnt(8)
; DEV int ltid() { int t = threadIdx.x; asm volatile("" : "+v"(t)); return t; }
; DEV unsigned cvt_pk4_fp8(f32x4 v) { unsigned r = 0; r = __builtin_amdgcn_cvt_pk_fp8_f32(v[0], v[1], r, false); r = __builtin_amdgcn_cvt_pk_fp8_f32(v[2], v[3], r, true); return r; }
; #define SBAR() __builtin_amdgcn_sched_barrier(0)
; #define PV_WAIT(n) do { asm volatile("s_waitcnt lgkmcnt(" #n ")" ::: "memory"); SBAR(); } while (0)
; DEV void fill_load(CParams& p, int wg, int slot, f32x4 (&ld)[4]) {
;   const FillDesc d = fill_decode(p, wg, slot); const int tid = ltid(), tx = tid & 15, ty = tid >> 4;
;   const float* sp = d.src + (long)(d.kh + 4 * ty) * d.ldsrc + d.n0 + 4 * tx;
; #pragma unroll
;   for (int r = 0; r < 4; ++r) ld[r] = *(const f32x4*)(sp + (long)r * d.ldsrc);
; }
; DEV void fill_write(const f32x4 (&ld)[4], int bufsel) {
;   extern __shared__ __attribute__((aligned(16))) char shm[];
;   unsigned* T = (unsigned*)(shm + FILL_LDS_OFF + bufsel * FILL_TB); const int tid = ltid(), tx = tid & 15, ty = tid >> 4;
;   constexpr float WS = (float)(1 << FP8_WSCALE_LOG2_);
; #pragma unroll
;   for (int j = 0; j < 4; ++j) T[(4 * tx + j) * 33 + ty] = cvt_pk4_fp8((f32x4){ld[0][j] * WS, ld[1][j] * WS, ld[2][j] * WS, ld[3][j] * WS});
; }
; DEV void pv_mma(f32x16& od, const VFrag& f, bf16x8 pa0, bf16x8 pa1, bf16x8 pa2, bf16x8 pa3) {
;     ...
;   __builtin_amdgcn_s_setprio(1);
;   od = __builtin_amdgcn_mfma_f32_32x32x16_bf16(pa0, PK(f.l0, f.h0), od, 0, 0, 0);
;   od = __builtin_amdgcn_mfma_f32_32x32x16_bf16(pa1, PK(f.l1, f.h1), od, 0, 0, 0);
;   od = __builtin_amdgcn_mfma_f32_32x32x16_bf16(pa2, PK(f.l2, f.h2), od, 0, 0, 0);
;   od = __builtin_amdgcn_mfma_f32_32x32x16_bf16(pa3, PK(f.l3, f.h3), od, 0, 0, 0);
;   __builtin_amdgcn_s_setprio(0);
;     ...
; }
; DEV void pv_d0(f32x16* o, int vb, bf16x8 pa0, bf16x8 pa1, bf16x8 pa2, bf16x8 pa3) {
;   VFrag fa, fb;
;   pv_read<0>(fa, vb);
;   pv_read<1>(fb, vb); PV_WAIT(8); pv_mma(o[0], fa, pa0, pa1, pa2, pa3); SBAR();
;   pv_read<2>(fa, vb); PV_WAIT(8); pv_mma(o[1], fb, pa0, pa1, pa2, pa3); SBAR();
;   pv_read<3>(fb, vb); PV_WAIT(8); pv_mma(o[2], fa, pa0, pa1, pa2, pa3); SBAR();
;   PV_WAIT(0); pv_mma(o[3], fb, pa0, pa1, pa2, pa3);
; }
	s_setprio 1
	v_mfma_f32_32x32x16_bf16 v[50:65], v[70:73], v[86:89], v[50:65]
	v_mfma_f32_32x32x16_bf16 v[50:65], v[74:77], v[90:93], v[50:65]
	v_mfma_f32_32x32x16_bf16 v[50:65], v[78:81], v[94:97], v[50:65]
	v_mfma_f32_32x32x16_bf16 v[50:65], v[82:85], v[224:227], v[50:65]
	s_setprio 0
	ds_read_b64_tr_b16 v[86:87], v66 offset:0x400
	ds_read_b64_tr_b16 v[88:89], v66 offset:0xc00
	ds_read_b64_tr_b16 v[90:91], v66 offset:0x1400
	ds_read_b64_tr_b16 v[92:93], v66 offset:0x1c00
	ds_read_b64_tr_b16 v[94:95], v66 offset:0x2400
	ds_read_b64_tr_b16 v[96:97], v66 offset:0x2c00
	ds_read_b64_tr_b16 v[224:225], v66 offset:0x3400
	ds_read_b64_tr_b16 v[226:227], v66 offset:0x3c00
	s_waitcnt lgkmcnt(8)
	s_setprio 1
	v_mfma_f32_32x32x16_bf16 v[34:49], v[70:73], v[228:231], v[34:49]
	v_mfma_f32_32x32x16_bf16 v[34:49], v[74:77], v[232:235], v[34:49]
	v_mfma_f32_32x32x16_bf16 v[34:49], v[78:81], v[236:239], v[34:49]
	v_mfma_f32_32x32x16_bf16 v[34:49], v[82:85], v[240:243], v[34:49]
	s_setprio 0
	ds_read_b64_tr_b16 v[228:229], v66 offset:0x600
	ds_read_b64_tr_b16 v[230:231], v66 offset:0xe00
	ds_read_b64_tr_b16 v[232:233], v66 offset:0x1600
	ds_read_b64_tr_b16 v[234:235], v66 offset:0x1e00
	ds_read_b64_tr_b16 v[236:237], v66 offset:0x2600
	ds_read_b64_tr_b16 v[238:239], v66 offset:0x2e00
	ds_read_b64_tr_b16 v[240:241], v66 offset:0x3600
	ds_read_b64_tr_b16 v[242:243], v66 offset:0x3e00
	s_waitcnt lgkmcnt(8)
	s_setprio 1
	v_mfma_f32_32x32x16_bf16 v[18:33], v[70:73], v[86:89], v[18:33]
	v_mfma_f32_32x32x16_bf16 v[18:33], v[74:77], v[90:93], v[18:33]
	v_mfma_f32_32x32x16_bf16 v[18:33], v[78:81], v[94:97], v[18:33]
	v_mfma_f32_32x32x16_bf16 v[18:33], v[82:85], v[224:227], v[18:33]
	s_setprio 0
	s_waitcnt lgkmcnt(0)
	s_setprio 1
	v_mfma_f32_32x32x16_bf16 v[2:17], v[70:73], v[228:231], v[2:17]
	v_mfma_f32_32x32x16_bf16 v[2:17], v[74:77], v[232:235], v[2:17]
	v_mfma_f32_32x32x16_bf16 v[2:17], v[78:81], v[236:239], v[2:17]
	v_mfma_f32_32x32x16_bf16 v[2:17], v[82:85], v[240:243], v[2:17]
	s_setprio 0
	s_cmp_gt_u32 s38, 61
	s_cbranch_scc1 .LBB0_1126
	s_mul_i32 s56, s37, 0x2200
	s_cmp_eq_u32 s35, 59
	v_add_u32_e32 v66, s56, v245
	ds_write2_b32 v66, v168, v169 offset1:33
	ds_write2_b32 v66, v170, v171 offset0:66 offset1:99
	s_cbranch_scc1 .LBB0_1126
	global_load_dwordx4 v[168:171], v248, s[62:63]
	global_load_dwordx4 v[172:175], v249, s[62:63]
	global_load_dwordx4 v[176:179], v250, s[62:63]
	global_load_dwordx4 v[180:183], v251, s[62:63]
	s_add_u32 s62, s62, 0x800000
	s_addc_u32 s63, s63, 0
